# in-proj gate epilogue: the u8 merge gates are consumed three phases later, so their 16 stores carry the nt hint to leave cache capacity to the projection columns the next phase reads; plus previous ch
# speedup vs baseline: 1.0067x; 1.0067x over previous
;     __device__ __forceinline__ void operator()(const AccT& acc, const gm::GUnit& u, int wr, int wc, int fr, int fq) const {
;     ...
;         if (u.sub == 1) {
;             const float* bp = bg + u.pn * 256 + wc * 32 + 8 * fq;
;             f32x4 bb[2][2];
; #pragma unroll
;             for (int bj = 0; bj < 2; ++bj) { bb[bj][0] = *(const f32x4*)(bp + bj * 128); bb[bj][1] = *(const f32x4*)(bp + bj * 128 + 4); }
;             __builtin_amdgcn_sched_barrier(0);
; #pragma unroll
;             for (int bj = 0; bj < 2; ++bj) {
;                 const f32x4 b0 = bb[bj][0], b1 = bb[bj][1];
; #pragma unroll
;                 for (int ai = 0; ai < 2; ++ai)
; #pragma unroll
;                     for (int m = 0; m < 4; ++m) {
;                         const int row = u.pm * 256 + ai * 128 + wr * 64 + m * 16 + fr;
;                         f32x4 v0 = (acc[ai][bj][m][0] + b0) * -1.4426950408889634f, v1 = (acc[ai][bj][m][1] + b1) * -1.4426950408889634f;
; #pragma unroll
;                         for (int j = 0; j < 4; ++j) { v0[j] = __builtin_amdgcn_exp2f(v0[j]); v1[j] = __builtin_amdgcn_exp2f(v1[j]); }
;                         v0 = v0 + 1.f; v1 = v1 + 1.f;
; #pragma unroll
;                         for (int j = 0; j < 4; ++j) { v0[j] = __builtin_amdgcn_rcpf(v0[j]); v1[j] = __builtin_amdgcn_rcpf(v1[j]); }
;                         v0 = v0 * 255.f + 0.5f; v1 = v1 * 255.f + 0.5f;
;                         unsigned q[8];
; #pragma unroll
;                         for (int j = 0; j < 4; ++j) { q[j] = max((unsigned)v0[j], 1u); q[4 + j] = max((unsigned)v1[j], 1u); }
;                         u32x2 w; w.x = q[0] | (q[1] << 8) | (q[2] << 16) | (q[3] << 24); w.y = q[4] | (q[5] << 8) | (q[6] << 16) | (q[7] << 24);
;                         *(u32x2*)(G8 + (size_t)row * INW + u.pn * 256 + bj * 128 + wc * 32 + 8 * fq) = w;
;                     }
.LBB0_263:
	s_and_b64 vcc, exec, s[8:9]
	s_cbranch_vccz .LBB0_237
	s_lshl_b32 s18, s74, 8
	s_ashr_i32 s19, s18, 31
	s_lshl_b64 s[0:1], s[18:19], 2
	s_add_u32 s0, s88, s0
	v_lshlrev_b32_e32 v148, 3, v203
	s_addc_u32 s1, s89, s1
	v_ashrrev_i32_e32 v149, 31, v148
	v_lshl_add_u64 v[134:135], v[148:149], 2, s[0:1]
	global_load_dwordx4 v[138:141], v[134:135], off offset:16
	global_load_dwordx4 v[142:145], v[134:135], off
	global_load_dwordx4 v[130:133], v[134:135], off offset:528
	s_nop 0
	global_load_dwordx4 v[134:137], v[134:135], off offset:512
	s_waitcnt vmcnt(0)
	v_pk_add_f32 v[122:123], v[122:123], v[138:139]
	v_pk_add_f32 v[126:127], v[126:127], v[142:143]
	v_pk_add_f32 v[124:125], v[124:125], v[140:141]
	v_pk_mul_f32 v[122:123], v[122:123], s[6:7] op_sel_hi:[1,0]
	v_pk_mul_f32 v[126:127], v[126:127], s[6:7] op_sel_hi:[1,0]
	v_pk_mul_f32 v[124:125], v[124:125], s[6:7] op_sel_hi:[1,0]
	v_exp_f32_e32 v122, v122
	v_exp_f32_e32 v123, v123
	v_exp_f32_e32 v126, v126
	v_exp_f32_e32 v127, v127
	v_exp_f32_e32 v124, v124
	v_exp_f32_e32 v125, v125
	v_pk_add_f32 v[114:115], v[114:115], v[138:139]
	v_pk_add_f32 v[128:129], v[128:129], v[144:145]
	v_pk_mul_f32 v[114:115], v[114:115], s[6:7] op_sel_hi:[1,0]
	v_pk_add_f32 v[122:123], v[122:123], 1.0 op_sel_hi:[1,0]
	v_exp_f32_e32 v114, v114
	v_exp_f32_e32 v115, v115
	v_pk_mul_f32 v[128:129], v[128:129], s[6:7] op_sel_hi:[1,0]
	v_pk_add_f32 v[126:127], v[126:127], 1.0 op_sel_hi:[1,0]
	v_pk_add_f32 v[124:125], v[124:125], 1.0 op_sel_hi:[1,0]
	v_rcp_f32_e32 v122, v122
	v_rcp_f32_e32 v123, v123
	v_exp_f32_e32 v128, v128
	v_exp_f32_e32 v129, v129
	v_rcp_f32_e32 v126, v126
	v_rcp_f32_e32 v127, v127
	v_rcp_f32_e32 v124, v124
	v_rcp_f32_e32 v125, v125
	v_pk_add_f32 v[120:121], v[120:121], v[144:145]
	v_pk_add_f32 v[116:117], v[116:117], v[140:141]
	v_pk_mul_f32 v[120:121], v[120:121], s[6:7] op_sel_hi:[1,0]
	v_pk_mul_f32 v[116:117], v[116:117], s[6:7] op_sel_hi:[1,0]
	v_pk_add_f32 v[114:115], v[114:115], 1.0 op_sel_hi:[1,0]
	v_exp_f32_e32 v120, v120
	v_exp_f32_e32 v121, v121
	v_exp_f32_e32 v116, v116
	v_exp_f32_e32 v117, v117
	v_rcp_f32_e32 v114, v114
	v_fma_f32 v122, v122, s33, 0.5
	v_fma_f32 v123, v123, s33, 0.5
	v_pk_add_f32 v[128:129], v[128:129], 1.0 op_sel_hi:[1,0]
	v_fma_f32 v126, v126, s33, 0.5
	v_cvt_u32_f32_e32 v122, v122
	v_fma_f32 v127, v127, s33, 0.5
	v_cvt_u32_f32_e32 v123, v123
	v_fma_f32 v124, v124, s33, 0.5
	v_fma_f32 v125, v125, s33, 0.5
	v_pk_add_f32 v[118:119], v[118:119], v[142:143]
	v_rcp_f32_e32 v128, v128
	v_rcp_f32_e32 v129, v129
	v_cvt_u32_f32_e32 v126, v126
	v_cvt_u32_f32_e32 v127, v127
	v_cvt_u32_f32_e32 v124, v124
	v_cvt_u32_f32_e32 v125, v125
	v_pk_mul_f32 v[118:119], v[118:119], s[6:7] op_sel_hi:[1,0]
	v_pk_add_f32 v[120:121], v[120:121], 1.0 op_sel_hi:[1,0]
	v_exp_f32_e32 v118, v118
	v_exp_f32_e32 v119, v119
	v_pk_add_f32 v[116:117], v[116:117], 1.0 op_sel_hi:[1,0]
	v_rcp_f32_e32 v115, v115
	v_fma_f32 v114, v114, s33, 0.5
	s_lshl_b32 s0, s72, 8
	v_rcp_f32_e32 v120, v120
	v_rcp_f32_e32 v116, v116
	v_rcp_f32_e32 v117, v117
	v_cvt_u32_f32_e32 v114, v114
	v_pk_add_f32 v[106:107], v[106:107], v[138:139]
	v_max_u32_e32 v122, 1, v122
	v_max_u32_e32 v123, 1, v123
	s_add_i32 s0, s0, s82
	v_pk_mul_f32 v[106:107], v[106:107], s[6:7] op_sel_hi:[1,0]
	v_max_u32_e32 v126, 1, v126
	v_max_u32_e32 v127, 1, v127
	v_fma_f32 v128, v128, s33, 0.5
	v_fma_f32 v129, v129, s33, 0.5
	v_max_u32_sdwa v150, v124, v228 dst_sel:WORD_1 dst_unused:UNUSED_PAD src0_sel:DWORD src1_sel:DWORD
	v_max_u32_sdwa v125, v125, v228 dst_sel:BYTE_3 dst_unused:UNUSED_PAD src0_sel:DWORD src1_sel:DWORD
	v_add_u32_e32 v124, s0, v201
	v_lshl_or_b32 v122, v123, 8, v122
	v_exp_f32_e32 v106, v106
	v_exp_f32_e32 v107, v107
	v_cvt_u32_f32_e32 v128, v128
	v_cvt_u32_f32_e32 v129, v129
	v_lshl_or_b32 v126, v127, 8, v126
	v_or3_b32 v127, v122, v150, v125
	v_ashrrev_i32_e32 v125, 31, v124
	v_pk_add_f32 v[118:119], v[118:119], 1.0 op_sel_hi:[1,0]
	v_fma_f32 v115, v115, s33, 0.5
	v_lshlrev_b64 v[122:123], 12, v[124:125]
	v_rcp_f32_e32 v118, v118
	v_rcp_f32_e32 v119, v119
	v_cvt_u32_f32_e32 v115, v115
	v_max_u32_e32 v125, 1, v114
	v_fma_f32 v114, v120, s33, 0.5
	v_fma_f32 v116, v116, s33, 0.5
	v_fma_f32 v117, v117, s33, 0.5
	v_lshl_add_u64 v[122:123], s[46:47], 0, v[122:123]
	v_rcp_f32_e32 v121, v121
	v_cvt_u32_f32_e32 v114, v114
	v_cvt_u32_f32_e32 v116, v116
	v_cvt_u32_f32_e32 v117, v117
	v_pk_add_f32 v[112:113], v[112:113], v[144:145]
	v_pk_add_f32 v[108:109], v[108:109], v[140:141]
	v_lshl_add_u64 v[122:123], v[122:123], 0, s[18:19]
	v_pk_mul_f32 v[112:113], v[112:113], s[6:7] op_sel_hi:[1,0]
	v_pk_mul_f32 v[108:109], v[108:109], s[6:7] op_sel_hi:[1,0]
	v_pk_add_f32 v[106:107], v[106:107], 1.0 op_sel_hi:[1,0]
	v_max_u32_sdwa v128, v128, v228 dst_sel:WORD_1 dst_unused:UNUSED_PAD src0_sel:DWORD src1_sel:DWORD
	v_max_u32_sdwa v129, v129, v228 dst_sel:BYTE_3 dst_unused:UNUSED_PAD src0_sel:DWORD src1_sel:DWORD
	v_lshl_add_u64 v[122:123], v[122:123], 0, s[48:49]
	v_exp_f32_e32 v112, v112
	v_exp_f32_e32 v113, v113
	v_exp_f32_e32 v108, v108
	v_exp_f32_e32 v109, v109
	v_rcp_f32_e32 v106, v106
	v_or3_b32 v126, v126, v128, v129
	v_lshl_add_u64 v[122:123], v[122:123], 0, v[148:149]
	v_fma_f32 v118, v118, s33, 0.5
	v_fma_f32 v119, v119, s33, 0.5
	v_max_u32_e32 v115, 1, v115
	global_store_dwordx2 v[122:123], v[126:127], off nt
	v_cvt_u32_f32_e32 v118, v118
	v_cvt_u32_f32_e32 v119, v119
	v_fma_f32 v120, v121, s33, 0.5
	v_max_u32_sdwa v121, v114, v228 dst_sel:WORD_1 dst_unused:UNUSED_PAD src0_sel:DWORD src1_sel:DWORD
	v_max_u32_sdwa v126, v116, v228 dst_sel:WORD_1 dst_unused:UNUSED_PAD src0_sel:DWORD src1_sel:DWORD
;     __device__ __forceinline__ void operator()(const AccT& acc, const gm::GUnit& u, int wr, int wc, int fr, int fq) const {
;     ...
;                     for (int m = 0; m < 4; ++m) {
;                         const int row = u.pm * 256 + ai * 128 + wr * 64 + m * 16 + fr;
;                         f32x4 v0 = (acc[ai][bj][m][0] + b0) * -1.4426950408889634f, v1 = (acc[ai][bj][m][1] + b1) * -1.4426950408889634f;
; #pragma unroll
;                         for (int j = 0; j < 4; ++j) { v0[j] = __builtin_amdgcn_exp2f(v0[j]); v1[j] = __builtin_amdgcn_exp2f(v1[j]); }
;                         v0 = v0 + 1.f; v1 = v1 + 1.f;
; #pragma unroll
;                         for (int j = 0; j < 4; ++j) { v0[j] = __builtin_amdgcn_rcpf(v0[j]); v1[j] = __builtin_amdgcn_rcpf(v1[j]); }
;                         v0 = v0 * 255.f + 0.5f; v1 = v1 * 255.f + 0.5f;
;                         unsigned q[8];
; #pragma unroll
;                         for (int j = 0; j < 4; ++j) { q[j] = max((unsigned)v0[j], 1u); q[4 + j] = max((unsigned)v1[j], 1u); }
;                         u32x2 w; w.x = q[0] | (q[1] << 8) | (q[2] << 16) | (q[3] << 24); w.y = q[4] | (q[5] << 8) | (q[6] << 16) | (q[7] << 24);
;                         *(u32x2*)(G8 + (size_t)row * INW + u.pn * 256 + bj * 128 + wc * 32 + 8 * fq) = w;
;                     }
	v_max_u32_sdwa v117, v117, v228 dst_sel:BYTE_3 dst_unused:UNUSED_PAD src0_sel:DWORD src1_sel:DWORD
	v_add_u32_e32 v114, 16, v124
	v_lshl_or_b32 v115, v115, 8, v125
	v_pk_add_f32 v[110:111], v[110:111], v[142:143]
	v_cvt_u32_f32_e32 v120, v120
	v_or3_b32 v117, v115, v126, v117
	v_ashrrev_i32_e32 v115, 31, v114
	v_pk_mul_f32 v[110:111], v[110:111], s[6:7] op_sel_hi:[1,0]
	v_lshlrev_b64 v[114:115], 12, v[114:115]
	v_exp_f32_e32 v110, v110
	v_exp_f32_e32 v111, v111
	v_pk_add_f32 v[112:113], v[112:113], 1.0 op_sel_hi:[1,0]
	v_pk_add_f32 v[108:109], v[108:109], 1.0 op_sel_hi:[1,0]
	v_rcp_f32_e32 v107, v107
	v_fma_f32 v106, v106, s33, 0.5
	v_lshl_add_u64 v[114:115], s[46:47], 0, v[114:115]
	v_rcp_f32_e32 v112, v112
	v_rcp_f32_e32 v108, v108
	v_rcp_f32_e32 v109, v109
	v_cvt_u32_f32_e32 v106, v106
	v_pk_add_f32 v[98:99], v[98:99], v[138:139]
	v_max_u32_e32 v118, 1, v118
	v_max_u32_e32 v119, 1, v119
	v_lshl_add_u64 v[114:115], v[114:115], 0, s[18:19]
	v_pk_mul_f32 v[98:99], v[98:99], s[6:7] op_sel_hi:[1,0]
	v_max_u32_sdwa v116, v120, v228 dst_sel:BYTE_3 dst_unused:UNUSED_PAD src0_sel:DWORD src1_sel:DWORD
	v_lshl_or_b32 v118, v119, 8, v118
	v_lshl_add_u64 v[114:115], v[114:115], 0, s[48:49]
	v_exp_f32_e32 v98, v98
	v_exp_f32_e32 v99, v99
	v_or3_b32 v116, v118, v121, v116
	v_lshl_add_u64 v[114:115], v[114:115], 0, v[148:149]
	v_pk_add_f32 v[110:111], v[110:111], 1.0 op_sel_hi:[1,0]
	v_fma_f32 v107, v107, s33, 0.5
	global_store_dwordx2 v[114:115], v[116:117], off nt
	v_rcp_f32_e32 v110, v110
	v_rcp_f32_e32 v111, v111
	v_cvt_u32_f32_e32 v107, v107
	v_max_u32_e32 v116, 1, v106
	v_fma_f32 v106, v112, s33, 0.5
	v_fma_f32 v108, v108, s33, 0.5
	v_fma_f32 v109, v109, s33, 0.5
	v_rcp_f32_e32 v113, v113
	v_cvt_u32_f32_e32 v106, v106
	v_cvt_u32_f32_e32 v108, v108
	v_cvt_u32_f32_e32 v109, v109
	v_pk_add_f32 v[104:105], v[104:105], v[144:145]
	v_pk_add_f32 v[100:101], v[100:101], v[140:141]
	v_pk_mul_f32 v[104:105], v[104:105], s[6:7] op_sel_hi:[1,0]
	v_pk_mul_f32 v[100:101], v[100:101], s[6:7] op_sel_hi:[1,0]
	v_pk_add_f32 v[98:99], v[98:99], 1.0 op_sel_hi:[1,0]
	v_exp_f32_e32 v104, v104
	v_exp_f32_e32 v105, v105
	v_exp_f32_e32 v100, v100
	v_exp_f32_e32 v101, v101
	v_rcp_f32_e32 v98, v98
	v_fma_f32 v110, v110, s33, 0.5
	v_fma_f32 v111, v111, s33, 0.5
	v_max_u32_e32 v107, 1, v107
	v_cvt_u32_f32_e32 v110, v110
	v_cvt_u32_f32_e32 v111, v111
	v_fma_f32 v112, v113, s33, 0.5
	v_max_u32_sdwa v113, v106, v228 dst_sel:WORD_1 dst_unused:UNUSED_PAD src0_sel:DWORD src1_sel:DWORD
	v_max_u32_sdwa v117, v108, v228 dst_sel:WORD_1 dst_unused:UNUSED_PAD src0_sel:DWORD src1_sel:DWORD
	v_max_u32_sdwa v109, v109, v228 dst_sel:BYTE_3 dst_unused:UNUSED_PAD src0_sel:DWORD src1_sel:DWORD
	v_add_u32_e32 v106, 32, v124
	v_lshl_or_b32 v107, v107, 8, v116
	v_pk_add_f32 v[102:103], v[102:103], v[142:143]
	v_cvt_u32_f32_e32 v112, v112
	v_or3_b32 v109, v107, v117, v109
	v_ashrrev_i32_e32 v107, 31, v106
	v_pk_mul_f32 v[102:103], v[102:103], s[6:7] op_sel_hi:[1,0]
	v_lshlrev_b64 v[106:107], 12, v[106:107]
	v_exp_f32_e32 v102, v102
	v_exp_f32_e32 v103, v103
	v_pk_add_f32 v[104:105], v[104:105], 1.0 op_sel_hi:[1,0]
	v_pk_add_f32 v[100:101], v[100:101], 1.0 op_sel_hi:[1,0]
	v_rcp_f32_e32 v99, v99
	v_fma_f32 v98, v98, s33, 0.5
	v_lshl_add_u64 v[106:107], s[46:47], 0, v[106:107]
	v_rcp_f32_e32 v104, v104
	v_rcp_f32_e32 v100, v100
	v_rcp_f32_e32 v101, v101
	v_cvt_u32_f32_e32 v98, v98
	v_pk_add_f32 v[90:91], v[90:91], v[138:139]
	v_max_u32_e32 v110, 1, v110
	v_max_u32_e32 v111, 1, v111
	v_lshl_add_u64 v[106:107], v[106:107], 0, s[18:19]
	v_pk_mul_f32 v[90:91], v[90:91], s[6:7] op_sel_hi:[1,0]
	v_max_u32_sdwa v108, v112, v228 dst_sel:BYTE_3 dst_unused:UNUSED_PAD src0_sel:DWORD src1_sel:DWORD
	v_lshl_or_b32 v110, v111, 8, v110
	v_lshl_add_u64 v[106:107], v[106:107], 0, s[48:49]
	v_exp_f32_e32 v90, v90
	v_exp_f32_e32 v91, v91
	v_or3_b32 v108, v110, v113, v108
	v_lshl_add_u64 v[106:107], v[106:107], 0, v[148:149]
	v_pk_add_f32 v[102:103], v[102:103], 1.0 op_sel_hi:[1,0]
	v_fma_f32 v99, v99, s33, 0.5
	global_store_dwordx2 v[106:107], v[108:109], off nt
	v_rcp_f32_e32 v102, v102
	v_rcp_f32_e32 v103, v103
	v_cvt_u32_f32_e32 v99, v99
	v_max_u32_e32 v108, 1, v98
	v_fma_f32 v98, v104, s33, 0.5
	v_fma_f32 v100, v100, s33, 0.5
	v_fma_f32 v101, v101, s33, 0.5
	v_rcp_f32_e32 v105, v105
	v_cvt_u32_f32_e32 v98, v98
	v_cvt_u32_f32_e32 v100, v100
	v_cvt_u32_f32_e32 v101, v101
	v_pk_add_f32 v[96:97], v[96:97], v[144:145]
	v_pk_add_f32 v[92:93], v[92:93], v[140:141]
	v_pk_mul_f32 v[96:97], v[96:97], s[6:7] op_sel_hi:[1,0]
	v_pk_mul_f32 v[92:93], v[92:93], s[6:7] op_sel_hi:[1,0]
	v_pk_add_f32 v[90:91], v[90:91], 1.0 op_sel_hi:[1,0]
	v_exp_f32_e32 v96, v96
	v_exp_f32_e32 v97, v97
	v_exp_f32_e32 v92, v92
	v_exp_f32_e32 v93, v93
	v_rcp_f32_e32 v90, v90
	v_fma_f32 v102, v102, s33, 0.5
	v_fma_f32 v103, v103, s33, 0.5
	v_max_u32_e32 v99, 1, v99
	v_cvt_u32_f32_e32 v102, v102
	v_cvt_u32_f32_e32 v103, v103
	v_fma_f32 v104, v105, s33, 0.5
	v_max_u32_sdwa v105, v98, v228 dst_sel:WORD_1 dst_unused:UNUSED_PAD src0_sel:DWORD src1_sel:DWORD
	v_max_u32_sdwa v109, v100, v228 dst_sel:WORD_1 dst_unused:UNUSED_PAD src0_sel:DWORD src1_sel:DWORD
	v_max_u32_sdwa v101, v101, v228 dst_sel:BYTE_3 dst_unused:UNUSED_PAD src0_sel:DWORD src1_sel:DWORD
	v_add_u32_e32 v98, 48, v124
	v_lshl_or_b32 v99, v99, 8, v108
	v_pk_add_f32 v[94:95], v[94:95], v[142:143]
	v_cvt_u32_f32_e32 v104, v104
	v_or3_b32 v101, v99, v109, v101
	v_ashrrev_i32_e32 v99, 31, v98
	v_pk_mul_f32 v[94:95], v[94:95], s[6:7] op_sel_hi:[1,0]
	v_lshlrev_b64 v[98:99], 12, v[98:99]
	v_exp_f32_e32 v94, v94
	v_exp_f32_e32 v95, v95
	v_pk_add_f32 v[96:97], v[96:97], 1.0 op_sel_hi:[1,0]
;     __device__ __forceinline__ void operator()(const AccT& acc, const gm::GUnit& u, int wr, int wc, int fr, int fq) const {
;     ...
;                     for (int m = 0; m < 4; ++m) {
;                         const int row = u.pm * 256 + ai * 128 + wr * 64 + m * 16 + fr;
;                         f32x4 v0 = (acc[ai][bj][m][0] + b0) * -1.4426950408889634f, v1 = (acc[ai][bj][m][1] + b1) * -1.4426950408889634f;
; #pragma unroll
;                         for (int j = 0; j < 4; ++j) { v0[j] = __builtin_amdgcn_exp2f(v0[j]); v1[j] = __builtin_amdgcn_exp2f(v1[j]); }
;                         v0 = v0 + 1.f; v1 = v1 + 1.f;
; #pragma unroll
;                         for (int j = 0; j < 4; ++j) { v0[j] = __builtin_amdgcn_rcpf(v0[j]); v1[j] = __builtin_amdgcn_rcpf(v1[j]); }
;                         v0 = v0 * 255.f + 0.5f; v1 = v1 * 255.f + 0.5f;
;                         unsigned q[8];
; #pragma unroll
;                         for (int j = 0; j < 4; ++j) { q[j] = max((unsigned)v0[j], 1u); q[4 + j] = max((unsigned)v1[j], 1u); }
;                         u32x2 w; w.x = q[0] | (q[1] << 8) | (q[2] << 16) | (q[3] << 24); w.y = q[4] | (q[5] << 8) | (q[6] << 16) | (q[7] << 24);
;                         *(u32x2*)(G8 + (size_t)row * INW + u.pn * 256 + bj * 128 + wc * 32 + 8 * fq) = w;
;                     }
	v_pk_add_f32 v[92:93], v[92:93], 1.0 op_sel_hi:[1,0]
	v_rcp_f32_e32 v91, v91
	v_fma_f32 v90, v90, s33, 0.5
	v_lshl_add_u64 v[98:99], s[46:47], 0, v[98:99]
	v_rcp_f32_e32 v96, v96
	v_rcp_f32_e32 v92, v92
	v_rcp_f32_e32 v93, v93
	v_cvt_u32_f32_e32 v90, v90
	v_pk_add_f32 v[82:83], v[82:83], v[138:139]
	v_max_u32_e32 v102, 1, v102
	v_max_u32_e32 v103, 1, v103
	v_lshl_add_u64 v[98:99], v[98:99], 0, s[18:19]
	v_pk_mul_f32 v[82:83], v[82:83], s[6:7] op_sel_hi:[1,0]
	v_max_u32_sdwa v100, v104, v228 dst_sel:BYTE_3 dst_unused:UNUSED_PAD src0_sel:DWORD src1_sel:DWORD
	v_lshl_or_b32 v102, v103, 8, v102
	v_lshl_add_u64 v[98:99], v[98:99], 0, s[48:49]
	v_exp_f32_e32 v82, v82
	v_exp_f32_e32 v83, v83
	v_or3_b32 v100, v102, v105, v100
	v_lshl_add_u64 v[98:99], v[98:99], 0, v[148:149]
	v_pk_add_f32 v[94:95], v[94:95], 1.0 op_sel_hi:[1,0]
	v_fma_f32 v91, v91, s33, 0.5
	global_store_dwordx2 v[98:99], v[100:101], off nt
	v_rcp_f32_e32 v94, v94
	v_rcp_f32_e32 v95, v95
	v_cvt_u32_f32_e32 v91, v91
	v_max_u32_e32 v100, 1, v90
	v_fma_f32 v90, v96, s33, 0.5
	v_fma_f32 v92, v92, s33, 0.5
	v_fma_f32 v93, v93, s33, 0.5
	v_rcp_f32_e32 v97, v97
	v_cvt_u32_f32_e32 v90, v90
	v_cvt_u32_f32_e32 v92, v92
	v_cvt_u32_f32_e32 v93, v93
	v_pk_add_f32 v[88:89], v[88:89], v[144:145]
	v_pk_add_f32 v[84:85], v[84:85], v[140:141]
	v_pk_mul_f32 v[88:89], v[88:89], s[6:7] op_sel_hi:[1,0]
	v_pk_mul_f32 v[84:85], v[84:85], s[6:7] op_sel_hi:[1,0]
	v_pk_add_f32 v[82:83], v[82:83], 1.0 op_sel_hi:[1,0]
	v_exp_f32_e32 v88, v88
	v_exp_f32_e32 v89, v89
	v_exp_f32_e32 v84, v84
	v_exp_f32_e32 v85, v85
	v_rcp_f32_e32 v82, v82
	v_fma_f32 v94, v94, s33, 0.5
	v_fma_f32 v95, v95, s33, 0.5
	v_max_u32_e32 v91, 1, v91
	v_cvt_u32_f32_e32 v94, v94
	v_cvt_u32_f32_e32 v95, v95
	v_fma_f32 v96, v97, s33, 0.5
	v_max_u32_sdwa v97, v90, v228 dst_sel:WORD_1 dst_unused:UNUSED_PAD src0_sel:DWORD src1_sel:DWORD
	v_max_u32_sdwa v101, v92, v228 dst_sel:WORD_1 dst_unused:UNUSED_PAD src0_sel:DWORD src1_sel:DWORD
	v_max_u32_sdwa v93, v93, v228 dst_sel:BYTE_3 dst_unused:UNUSED_PAD src0_sel:DWORD src1_sel:DWORD
	v_add_u32_e32 v90, 0x80, v124
	v_lshl_or_b32 v91, v91, 8, v100
	v_pk_add_f32 v[86:87], v[86:87], v[142:143]
	v_cvt_u32_f32_e32 v96, v96
	v_or3_b32 v93, v91, v101, v93
	v_ashrrev_i32_e32 v91, 31, v90
	v_pk_mul_f32 v[86:87], v[86:87], s[6:7] op_sel_hi:[1,0]
	v_lshlrev_b64 v[90:91], 12, v[90:91]
	v_exp_f32_e32 v86, v86
	v_exp_f32_e32 v87, v87
	v_pk_add_f32 v[88:89], v[88:89], 1.0 op_sel_hi:[1,0]
	v_pk_add_f32 v[84:85], v[84:85], 1.0 op_sel_hi:[1,0]
	v_rcp_f32_e32 v83, v83
	v_fma_f32 v82, v82, s33, 0.5
	v_lshl_add_u64 v[90:91], s[46:47], 0, v[90:91]
	v_rcp_f32_e32 v88, v88
	v_rcp_f32_e32 v84, v84
	v_rcp_f32_e32 v85, v85
	v_cvt_u32_f32_e32 v82, v82
	v_pk_add_f32 v[74:75], v[74:75], v[138:139]
	v_max_u32_e32 v94, 1, v94
	v_max_u32_e32 v95, 1, v95
	v_lshl_add_u64 v[90:91], v[90:91], 0, s[18:19]
	v_pk_mul_f32 v[74:75], v[74:75], s[6:7] op_sel_hi:[1,0]
	v_max_u32_sdwa v92, v96, v228 dst_sel:BYTE_3 dst_unused:UNUSED_PAD src0_sel:DWORD src1_sel:DWORD
	v_lshl_or_b32 v94, v95, 8, v94
	v_lshl_add_u64 v[90:91], v[90:91], 0, s[48:49]
	v_exp_f32_e32 v74, v74
	v_exp_f32_e32 v75, v75
	v_or3_b32 v92, v94, v97, v92
	v_lshl_add_u64 v[90:91], v[90:91], 0, v[148:149]
	v_pk_add_f32 v[86:87], v[86:87], 1.0 op_sel_hi:[1,0]
	v_fma_f32 v83, v83, s33, 0.5
	global_store_dwordx2 v[90:91], v[92:93], off nt
	v_rcp_f32_e32 v86, v86
	v_rcp_f32_e32 v87, v87
	v_cvt_u32_f32_e32 v83, v83
	v_max_u32_e32 v92, 1, v82
	v_fma_f32 v82, v88, s33, 0.5
	v_fma_f32 v84, v84, s33, 0.5
	v_fma_f32 v85, v85, s33, 0.5
	v_rcp_f32_e32 v89, v89
	v_cvt_u32_f32_e32 v82, v82
	v_cvt_u32_f32_e32 v84, v84
	v_cvt_u32_f32_e32 v85, v85
	v_pk_add_f32 v[80:81], v[80:81], v[144:145]
	v_pk_add_f32 v[76:77], v[76:77], v[140:141]
	v_pk_mul_f32 v[80:81], v[80:81], s[6:7] op_sel_hi:[1,0]
	v_pk_mul_f32 v[76:77], v[76:77], s[6:7] op_sel_hi:[1,0]
	v_pk_add_f32 v[74:75], v[74:75], 1.0 op_sel_hi:[1,0]
	v_exp_f32_e32 v80, v80
	v_exp_f32_e32 v81, v81
	v_exp_f32_e32 v76, v76
	v_exp_f32_e32 v77, v77
	v_rcp_f32_e32 v74, v74
	v_fma_f32 v86, v86, s33, 0.5
	v_fma_f32 v87, v87, s33, 0.5
	v_max_u32_e32 v83, 1, v83
	v_cvt_u32_f32_e32 v86, v86
	v_cvt_u32_f32_e32 v87, v87
	v_fma_f32 v88, v89, s33, 0.5
	v_max_u32_sdwa v89, v82, v228 dst_sel:WORD_1 dst_unused:UNUSED_PAD src0_sel:DWORD src1_sel:DWORD
	v_max_u32_sdwa v93, v84, v228 dst_sel:WORD_1 dst_unused:UNUSED_PAD src0_sel:DWORD src1_sel:DWORD
	v_max_u32_sdwa v85, v85, v228 dst_sel:BYTE_3 dst_unused:UNUSED_PAD src0_sel:DWORD src1_sel:DWORD
	v_add_u32_e32 v82, 0x90, v124
	v_lshl_or_b32 v83, v83, 8, v92
	v_pk_add_f32 v[78:79], v[78:79], v[142:143]
	v_cvt_u32_f32_e32 v88, v88
	v_or3_b32 v85, v83, v93, v85
	v_ashrrev_i32_e32 v83, 31, v82
	v_pk_mul_f32 v[78:79], v[78:79], s[6:7] op_sel_hi:[1,0]
	v_lshlrev_b64 v[82:83], 12, v[82:83]
	v_exp_f32_e32 v78, v78
	v_exp_f32_e32 v79, v79
	v_pk_add_f32 v[80:81], v[80:81], 1.0 op_sel_hi:[1,0]
	v_pk_add_f32 v[76:77], v[76:77], 1.0 op_sel_hi:[1,0]
	v_rcp_f32_e32 v75, v75
	v_fma_f32 v74, v74, s33, 0.5
	v_lshl_add_u64 v[82:83], s[46:47], 0, v[82:83]
	v_rcp_f32_e32 v80, v80
	v_rcp_f32_e32 v76, v76
	v_rcp_f32_e32 v77, v77
	v_cvt_u32_f32_e32 v74, v74
	v_pk_add_f32 v[66:67], v[66:67], v[138:139]
	v_max_u32_e32 v86, 1, v86
	v_max_u32_e32 v87, 1, v87
	v_lshl_add_u64 v[82:83], v[82:83], 0, s[18:19]
	v_pk_mul_f32 v[66:67], v[66:67], s[6:7] op_sel_hi:[1,0]
	v_max_u32_sdwa v84, v88, v228 dst_sel:BYTE_3 dst_unused:UNUSED_PAD src0_sel:DWORD src1_sel:DWORD
	v_lshl_or_b32 v86, v87, 8, v86
	v_lshl_add_u64 v[82:83], v[82:83], 0, s[48:49]
	v_exp_f32_e32 v66, v66
	v_exp_f32_e32 v67, v67
	v_or3_b32 v84, v86, v89, v84
;     __device__ __forceinline__ void operator()(const AccT& acc, const gm::GUnit& u, int wr, int wc, int fr, int fq) const {
;     ...
;                     for (int m = 0; m < 4; ++m) {
;                         const int row = u.pm * 256 + ai * 128 + wr * 64 + m * 16 + fr;
;                         f32x4 v0 = (acc[ai][bj][m][0] + b0) * -1.4426950408889634f, v1 = (acc[ai][bj][m][1] + b1) * -1.4426950408889634f;
; #pragma unroll
;                         for (int j = 0; j < 4; ++j) { v0[j] = __builtin_amdgcn_exp2f(v0[j]); v1[j] = __builtin_amdgcn_exp2f(v1[j]); }
;                         v0 = v0 + 1.f; v1 = v1 + 1.f;
; #pragma unroll
;                         for (int j = 0; j < 4; ++j) { v0[j] = __builtin_amdgcn_rcpf(v0[j]); v1[j] = __builtin_amdgcn_rcpf(v1[j]); }
;                         v0 = v0 * 255.f + 0.5f; v1 = v1 * 255.f + 0.5f;
;                         unsigned q[8];
; #pragma unroll
;                         for (int j = 0; j < 4; ++j) { q[j] = max((unsigned)v0[j], 1u); q[4 + j] = max((unsigned)v1[j], 1u); }
;                         u32x2 w; w.x = q[0] | (q[1] << 8) | (q[2] << 16) | (q[3] << 24); w.y = q[4] | (q[5] << 8) | (q[6] << 16) | (q[7] << 24);
;                         *(u32x2*)(G8 + (size_t)row * INW + u.pn * 256 + bj * 128 + wc * 32 + 8 * fq) = w;
;                     }
	v_lshl_add_u64 v[82:83], v[82:83], 0, v[148:149]
	v_pk_add_f32 v[78:79], v[78:79], 1.0 op_sel_hi:[1,0]
	v_fma_f32 v75, v75, s33, 0.5
	global_store_dwordx2 v[82:83], v[84:85], off nt
	v_rcp_f32_e32 v78, v78
	v_rcp_f32_e32 v79, v79
	v_cvt_u32_f32_e32 v75, v75
	v_max_u32_e32 v84, 1, v74
	v_fma_f32 v74, v80, s33, 0.5
	v_fma_f32 v76, v76, s33, 0.5
	v_fma_f32 v77, v77, s33, 0.5
	v_rcp_f32_e32 v81, v81
	v_cvt_u32_f32_e32 v74, v74
	v_cvt_u32_f32_e32 v76, v76
	v_cvt_u32_f32_e32 v77, v77
	v_pk_add_f32 v[72:73], v[72:73], v[144:145]
	v_pk_add_f32 v[68:69], v[68:69], v[140:141]
	v_pk_mul_f32 v[72:73], v[72:73], s[6:7] op_sel_hi:[1,0]
	v_pk_mul_f32 v[68:69], v[68:69], s[6:7] op_sel_hi:[1,0]
	v_pk_add_f32 v[66:67], v[66:67], 1.0 op_sel_hi:[1,0]
	v_exp_f32_e32 v72, v72
	v_exp_f32_e32 v73, v73
	v_exp_f32_e32 v68, v68
	v_exp_f32_e32 v69, v69
	v_rcp_f32_e32 v66, v66
	v_fma_f32 v78, v78, s33, 0.5
	v_fma_f32 v79, v79, s33, 0.5
	v_max_u32_e32 v75, 1, v75
	v_cvt_u32_f32_e32 v78, v78
	v_cvt_u32_f32_e32 v79, v79
	v_fma_f32 v80, v81, s33, 0.5
	v_max_u32_sdwa v81, v74, v228 dst_sel:WORD_1 dst_unused:UNUSED_PAD src0_sel:DWORD src1_sel:DWORD
	v_max_u32_sdwa v85, v76, v228 dst_sel:WORD_1 dst_unused:UNUSED_PAD src0_sel:DWORD src1_sel:DWORD
	v_max_u32_sdwa v77, v77, v228 dst_sel:BYTE_3 dst_unused:UNUSED_PAD src0_sel:DWORD src1_sel:DWORD
	v_add_u32_e32 v74, 0xa0, v124
	v_lshl_or_b32 v75, v75, 8, v84
	v_pk_add_f32 v[70:71], v[70:71], v[142:143]
	v_cvt_u32_f32_e32 v80, v80
	v_or3_b32 v77, v75, v85, v77
	v_ashrrev_i32_e32 v75, 31, v74
	v_pk_mul_f32 v[70:71], v[70:71], s[6:7] op_sel_hi:[1,0]
	v_lshlrev_b64 v[74:75], 12, v[74:75]
	v_exp_f32_e32 v70, v70
	v_exp_f32_e32 v71, v71
	v_pk_add_f32 v[72:73], v[72:73], 1.0 op_sel_hi:[1,0]
	v_pk_add_f32 v[68:69], v[68:69], 1.0 op_sel_hi:[1,0]
	v_rcp_f32_e32 v67, v67
	v_fma_f32 v66, v66, s33, 0.5
	v_lshl_add_u64 v[74:75], s[46:47], 0, v[74:75]
	v_rcp_f32_e32 v72, v72
	v_rcp_f32_e32 v68, v68
	v_rcp_f32_e32 v69, v69
	v_cvt_u32_f32_e32 v66, v66
	v_pk_add_f32 v[62:63], v[62:63], v[134:135]
	v_pk_add_f32 v[58:59], v[58:59], v[130:131]
	v_max_u32_e32 v78, 1, v78
	v_max_u32_e32 v79, 1, v79
	v_lshl_add_u64 v[74:75], v[74:75], 0, s[18:19]
	v_pk_mul_f32 v[62:63], v[62:63], s[6:7] op_sel_hi:[1,0]
	v_pk_mul_f32 v[58:59], v[58:59], s[6:7] op_sel_hi:[1,0]
	v_max_u32_sdwa v76, v80, v228 dst_sel:BYTE_3 dst_unused:UNUSED_PAD src0_sel:DWORD src1_sel:DWORD
	v_lshl_or_b32 v78, v79, 8, v78
	v_lshl_add_u64 v[74:75], v[74:75], 0, s[48:49]
	v_exp_f32_e32 v62, v62
	v_exp_f32_e32 v58, v58
	v_exp_f32_e32 v63, v63
	v_exp_f32_e32 v59, v59
	v_or3_b32 v76, v78, v81, v76
	v_lshl_add_u64 v[74:75], v[74:75], 0, v[148:149]
	v_pk_add_f32 v[70:71], v[70:71], 1.0 op_sel_hi:[1,0]
	v_fma_f32 v67, v67, s33, 0.5
	global_store_dwordx2 v[74:75], v[76:77], off nt
	v_rcp_f32_e32 v70, v70
	v_rcp_f32_e32 v71, v71
	v_cvt_u32_f32_e32 v67, v67
	v_max_u32_e32 v76, 1, v66
	v_fma_f32 v66, v72, s33, 0.5
	v_fma_f32 v68, v68, s33, 0.5
	v_fma_f32 v69, v69, s33, 0.5
	v_rcp_f32_e32 v73, v73
	v_cvt_u32_f32_e32 v66, v66
	v_cvt_u32_f32_e32 v68, v68
	v_cvt_u32_f32_e32 v69, v69
	v_pk_add_f32 v[64:65], v[64:65], v[136:137]
	v_pk_add_f32 v[60:61], v[60:61], v[132:133]
	v_pk_mul_f32 v[64:65], v[64:65], s[6:7] op_sel_hi:[1,0]
	v_pk_mul_f32 v[60:61], v[60:61], s[6:7] op_sel_hi:[1,0]
	v_pk_add_f32 v[62:63], v[62:63], 1.0 op_sel_hi:[1,0]
	v_pk_add_f32 v[58:59], v[58:59], 1.0 op_sel_hi:[1,0]
	v_exp_f32_e32 v64, v64
	v_exp_f32_e32 v65, v65
	v_exp_f32_e32 v60, v60
	v_exp_f32_e32 v61, v61
	v_rcp_f32_e32 v58, v58
	v_rcp_f32_e32 v63, v63
	v_pk_add_f32 v[54:55], v[54:55], v[134:135]
	v_pk_add_f32 v[50:51], v[50:51], v[130:131]
	v_fma_f32 v70, v70, s33, 0.5
	v_fma_f32 v71, v71, s33, 0.5
	v_max_u32_e32 v67, 1, v67
	v_pk_mul_f32 v[54:55], v[54:55], s[6:7] op_sel_hi:[1,0]
	v_pk_mul_f32 v[50:51], v[50:51], s[6:7] op_sel_hi:[1,0]
	v_cvt_u32_f32_e32 v70, v70
	v_cvt_u32_f32_e32 v71, v71
	v_fma_f32 v72, v73, s33, 0.5
	v_max_u32_sdwa v73, v66, v228 dst_sel:WORD_1 dst_unused:UNUSED_PAD src0_sel:DWORD src1_sel:DWORD
	v_max_u32_sdwa v77, v68, v228 dst_sel:WORD_1 dst_unused:UNUSED_PAD src0_sel:DWORD src1_sel:DWORD
	v_max_u32_sdwa v69, v69, v228 dst_sel:BYTE_3 dst_unused:UNUSED_PAD src0_sel:DWORD src1_sel:DWORD
	v_add_u32_e32 v66, 0xb0, v124
	v_lshl_or_b32 v67, v67, 8, v76
	v_exp_f32_e32 v54, v54
	v_exp_f32_e32 v50, v50
	v_exp_f32_e32 v55, v55
	v_exp_f32_e32 v51, v51
	v_cvt_u32_f32_e32 v72, v72
	v_or3_b32 v69, v67, v77, v69
	v_ashrrev_i32_e32 v67, 31, v66
	v_lshlrev_b64 v[66:67], 12, v[66:67]
	v_pk_add_f32 v[64:65], v[64:65], 1.0 op_sel_hi:[1,0]
	v_pk_add_f32 v[60:61], v[60:61], 1.0 op_sel_hi:[1,0]
	v_rcp_f32_e32 v62, v62
	v_rcp_f32_e32 v59, v59
	v_fma_f32 v58, v58, s33, 0.5
	v_fma_f32 v63, v63, s33, 0.5
	v_lshl_add_u64 v[66:67], s[46:47], 0, v[66:67]
	v_rcp_f32_e32 v64, v64
	v_rcp_f32_e32 v60, v60
	v_rcp_f32_e32 v65, v65
	v_rcp_f32_e32 v61, v61
	v_cvt_u32_f32_e32 v58, v58
	v_cvt_u32_f32_e32 v63, v63
	v_pk_add_f32 v[56:57], v[56:57], v[136:137]
	v_pk_add_f32 v[52:53], v[52:53], v[132:133]
	v_max_u32_e32 v70, 1, v70
	v_max_u32_e32 v71, 1, v71
	v_lshl_add_u64 v[66:67], v[66:67], 0, s[18:19]
	v_pk_mul_f32 v[56:57], v[56:57], s[6:7] op_sel_hi:[1,0]
	v_pk_mul_f32 v[52:53], v[52:53], s[6:7] op_sel_hi:[1,0]
	v_pk_add_f32 v[54:55], v[54:55], 1.0 op_sel_hi:[1,0]
	v_pk_add_f32 v[50:51], v[50:51], 1.0 op_sel_hi:[1,0]
	v_max_u32_sdwa v68, v72, v228 dst_sel:BYTE_3 dst_unused:UNUSED_PAD src0_sel:DWORD src1_sel:DWORD
	v_lshl_or_b32 v70, v71, 8, v70
	v_lshl_add_u64 v[66:67], v[66:67], 0, s[48:49]
	v_exp_f32_e32 v56, v56
	v_exp_f32_e32 v57, v57
	v_exp_f32_e32 v52, v52
	v_exp_f32_e32 v53, v53
	v_rcp_f32_e32 v50, v50
	v_rcp_f32_e32 v55, v55
;     __device__ __forceinline__ void operator()(const AccT& acc, const gm::GUnit& u, int wr, int wc, int fr, int fq) const {
;     ...
;                     for (int m = 0; m < 4; ++m) {
;                         const int row = u.pm * 256 + ai * 128 + wr * 64 + m * 16 + fr;
;                         f32x4 v0 = (acc[ai][bj][m][0] + b0) * -1.4426950408889634f, v1 = (acc[ai][bj][m][1] + b1) * -1.4426950408889634f;
; #pragma unroll
;                         for (int j = 0; j < 4; ++j) { v0[j] = __builtin_amdgcn_exp2f(v0[j]); v1[j] = __builtin_amdgcn_exp2f(v1[j]); }
;                         v0 = v0 + 1.f; v1 = v1 + 1.f;
; #pragma unroll
;                         for (int j = 0; j < 4; ++j) { v0[j] = __builtin_amdgcn_rcpf(v0[j]); v1[j] = __builtin_amdgcn_rcpf(v1[j]); }
;                         v0 = v0 * 255.f + 0.5f; v1 = v1 * 255.f + 0.5f;
;                         unsigned q[8];
; #pragma unroll
;                         for (int j = 0; j < 4; ++j) { q[j] = max((unsigned)v0[j], 1u); q[4 + j] = max((unsigned)v1[j], 1u); }
;                         u32x2 w; w.x = q[0] | (q[1] << 8) | (q[2] << 16) | (q[3] << 24); w.y = q[4] | (q[5] << 8) | (q[6] << 16) | (q[7] << 24);
;                         *(u32x2*)(G8 + (size_t)row * INW + u.pn * 256 + bj * 128 + wc * 32 + 8 * fq) = w;
;                     }
	v_pk_add_f32 v[46:47], v[46:47], v[134:135]
	v_pk_add_f32 v[42:43], v[42:43], v[130:131]
	v_or3_b32 v68, v70, v73, v68
	v_lshl_add_u64 v[66:67], v[66:67], 0, v[148:149]
	v_fma_f32 v62, v62, s33, 0.5
	v_fma_f32 v59, v59, s33, 0.5
	v_pk_mul_f32 v[46:47], v[46:47], s[6:7] op_sel_hi:[1,0]
	v_pk_mul_f32 v[42:43], v[42:43], s[6:7] op_sel_hi:[1,0]
	global_store_dwordx2 v[66:67], v[68:69], off nt
	v_cvt_u32_f32_e32 v62, v62
	v_cvt_u32_f32_e32 v59, v59
	v_max_u32_e32 v68, 1, v58
	v_max_u32_e32 v58, 1, v63
	v_fma_f32 v63, v64, s33, 0.5
	v_fma_f32 v60, v60, s33, 0.5
	v_fma_f32 v64, v65, s33, 0.5
	v_fma_f32 v61, v61, s33, 0.5
	v_exp_f32_e32 v46, v46
	v_exp_f32_e32 v42, v42
	v_exp_f32_e32 v47, v47
	v_exp_f32_e32 v43, v43
	v_cvt_u32_f32_e32 v63, v63
	v_cvt_u32_f32_e32 v60, v60
	v_cvt_u32_f32_e32 v64, v64
	v_cvt_u32_f32_e32 v61, v61
	v_pk_add_f32 v[56:57], v[56:57], 1.0 op_sel_hi:[1,0]
	v_pk_add_f32 v[52:53], v[52:53], 1.0 op_sel_hi:[1,0]
	v_rcp_f32_e32 v54, v54
	v_rcp_f32_e32 v51, v51
	v_fma_f32 v50, v50, s33, 0.5
	v_fma_f32 v55, v55, s33, 0.5
	v_rcp_f32_e32 v56, v56
	v_rcp_f32_e32 v52, v52
	v_rcp_f32_e32 v57, v57
	v_rcp_f32_e32 v53, v53
	v_cvt_u32_f32_e32 v50, v50
	v_cvt_u32_f32_e32 v55, v55
	v_pk_add_f32 v[48:49], v[48:49], v[136:137]
	v_pk_add_f32 v[44:45], v[44:45], v[132:133]
	v_max_u32_e32 v62, 1, v62
	v_max_u32_e32 v59, 1, v59
	v_pk_mul_f32 v[48:49], v[48:49], s[6:7] op_sel_hi:[1,0]
	v_pk_mul_f32 v[44:45], v[44:45], s[6:7] op_sel_hi:[1,0]
	v_pk_add_f32 v[46:47], v[46:47], 1.0 op_sel_hi:[1,0]
	v_pk_add_f32 v[42:43], v[42:43], 1.0 op_sel_hi:[1,0]
	v_max_u32_sdwa v63, v63, v228 dst_sel:WORD_1 dst_unused:UNUSED_PAD src0_sel:DWORD src1_sel:DWORD
	v_max_u32_sdwa v60, v60, v228 dst_sel:WORD_1 dst_unused:UNUSED_PAD src0_sel:DWORD src1_sel:DWORD
	v_max_u32_sdwa v64, v64, v228 dst_sel:BYTE_3 dst_unused:UNUSED_PAD src0_sel:DWORD src1_sel:DWORD
	v_max_u32_sdwa v61, v61, v228 dst_sel:BYTE_3 dst_unused:UNUSED_PAD src0_sel:DWORD src1_sel:DWORD
	v_lshl_or_b32 v58, v58, 8, v62
	v_lshl_or_b32 v59, v59, 8, v68
	v_exp_f32_e32 v48, v48
	v_exp_f32_e32 v49, v49
	v_exp_f32_e32 v44, v44
	v_exp_f32_e32 v45, v45
	v_rcp_f32_e32 v42, v42
	v_rcp_f32_e32 v47, v47
	v_pk_add_f32 v[38:39], v[38:39], v[134:135]
	v_pk_add_f32 v[34:35], v[34:35], v[130:131]
	v_or3_b32 v58, v58, v63, v64
	v_or3_b32 v59, v59, v60, v61
	v_fma_f32 v54, v54, s33, 0.5
	v_fma_f32 v51, v51, s33, 0.5
	v_pk_mul_f32 v[38:39], v[38:39], s[6:7] op_sel_hi:[1,0]
	v_pk_mul_f32 v[34:35], v[34:35], s[6:7] op_sel_hi:[1,0]
	global_store_dwordx2 v[122:123], v[58:59], off offset:128 nt
	v_cvt_u32_f32_e32 v54, v54
	v_cvt_u32_f32_e32 v51, v51
	v_max_u32_e32 v58, 1, v50
	v_max_u32_e32 v50, 1, v55
	v_fma_f32 v55, v56, s33, 0.5
	v_fma_f32 v52, v52, s33, 0.5
	v_fma_f32 v56, v57, s33, 0.5
	v_fma_f32 v53, v53, s33, 0.5
	v_exp_f32_e32 v38, v38
	v_exp_f32_e32 v34, v34
	v_exp_f32_e32 v39, v39
	v_exp_f32_e32 v35, v35
	v_cvt_u32_f32_e32 v55, v55
	v_cvt_u32_f32_e32 v52, v52
	v_cvt_u32_f32_e32 v56, v56
	v_cvt_u32_f32_e32 v53, v53
	v_pk_add_f32 v[48:49], v[48:49], 1.0 op_sel_hi:[1,0]
	v_pk_add_f32 v[44:45], v[44:45], 1.0 op_sel_hi:[1,0]
	v_rcp_f32_e32 v46, v46
	v_rcp_f32_e32 v43, v43
	v_fma_f32 v42, v42, s33, 0.5
	v_fma_f32 v47, v47, s33, 0.5
	v_rcp_f32_e32 v48, v48
	v_rcp_f32_e32 v44, v44
	v_rcp_f32_e32 v49, v49
	v_rcp_f32_e32 v45, v45
	v_cvt_u32_f32_e32 v42, v42
	v_cvt_u32_f32_e32 v47, v47
	v_pk_add_f32 v[40:41], v[40:41], v[136:137]
	v_pk_add_f32 v[36:37], v[36:37], v[132:133]
	v_max_u32_e32 v54, 1, v54
	v_max_u32_e32 v51, 1, v51
	v_pk_mul_f32 v[40:41], v[40:41], s[6:7] op_sel_hi:[1,0]
	v_pk_mul_f32 v[36:37], v[36:37], s[6:7] op_sel_hi:[1,0]
	v_pk_add_f32 v[38:39], v[38:39], 1.0 op_sel_hi:[1,0]
	v_pk_add_f32 v[34:35], v[34:35], 1.0 op_sel_hi:[1,0]
	v_max_u32_sdwa v55, v55, v228 dst_sel:WORD_1 dst_unused:UNUSED_PAD src0_sel:DWORD src1_sel:DWORD
	v_max_u32_sdwa v52, v52, v228 dst_sel:WORD_1 dst_unused:UNUSED_PAD src0_sel:DWORD src1_sel:DWORD
	v_max_u32_sdwa v56, v56, v228 dst_sel:BYTE_3 dst_unused:UNUSED_PAD src0_sel:DWORD src1_sel:DWORD
	v_max_u32_sdwa v53, v53, v228 dst_sel:BYTE_3 dst_unused:UNUSED_PAD src0_sel:DWORD src1_sel:DWORD
	v_lshl_or_b32 v50, v50, 8, v54
	v_lshl_or_b32 v51, v51, 8, v58
	v_exp_f32_e32 v40, v40
	v_exp_f32_e32 v41, v41
	v_exp_f32_e32 v36, v36
	v_exp_f32_e32 v37, v37
	v_rcp_f32_e32 v34, v34
	v_rcp_f32_e32 v39, v39
	v_pk_add_f32 v[30:31], v[30:31], v[134:135]
	v_pk_add_f32 v[26:27], v[26:27], v[130:131]
	v_or3_b32 v50, v50, v55, v56
	v_or3_b32 v51, v51, v52, v53
	v_fma_f32 v46, v46, s33, 0.5
	v_fma_f32 v43, v43, s33, 0.5
	v_pk_mul_f32 v[30:31], v[30:31], s[6:7] op_sel_hi:[1,0]
	v_pk_mul_f32 v[26:27], v[26:27], s[6:7] op_sel_hi:[1,0]
	global_store_dwordx2 v[114:115], v[50:51], off offset:128 nt
	v_cvt_u32_f32_e32 v46, v46
	v_cvt_u32_f32_e32 v43, v43
	v_max_u32_e32 v50, 1, v42
	v_max_u32_e32 v42, 1, v47
	v_fma_f32 v47, v48, s33, 0.5
	v_fma_f32 v44, v44, s33, 0.5
	v_fma_f32 v48, v49, s33, 0.5
	v_fma_f32 v45, v45, s33, 0.5
	v_exp_f32_e32 v30, v30
	v_exp_f32_e32 v26, v26
	v_exp_f32_e32 v31, v31
	v_exp_f32_e32 v27, v27
	v_cvt_u32_f32_e32 v47, v47
	v_cvt_u32_f32_e32 v44, v44
	v_cvt_u32_f32_e32 v48, v48
	v_cvt_u32_f32_e32 v45, v45
	v_pk_add_f32 v[40:41], v[40:41], 1.0 op_sel_hi:[1,0]
	v_pk_add_f32 v[36:37], v[36:37], 1.0 op_sel_hi:[1,0]
	v_rcp_f32_e32 v38, v38
	v_rcp_f32_e32 v35, v35
	v_fma_f32 v34, v34, s33, 0.5
	v_fma_f32 v39, v39, s33, 0.5
	v_rcp_f32_e32 v40, v40
	v_rcp_f32_e32 v36, v36
	v_rcp_f32_e32 v41, v41
	v_rcp_f32_e32 v37, v37
	v_cvt_u32_f32_e32 v34, v34
	v_cvt_u32_f32_e32 v39, v39
	v_pk_add_f32 v[32:33], v[32:33], v[136:137]
	v_pk_add_f32 v[28:29], v[28:29], v[132:133]
	v_max_u32_e32 v46, 1, v46
;     __device__ __forceinline__ void operator()(const AccT& acc, const gm::GUnit& u, int wr, int wc, int fr, int fq) const {
;     ...
;                     for (int m = 0; m < 4; ++m) {
;                         const int row = u.pm * 256 + ai * 128 + wr * 64 + m * 16 + fr;
;                         f32x4 v0 = (acc[ai][bj][m][0] + b0) * -1.4426950408889634f, v1 = (acc[ai][bj][m][1] + b1) * -1.4426950408889634f;
; #pragma unroll
;                         for (int j = 0; j < 4; ++j) { v0[j] = __builtin_amdgcn_exp2f(v0[j]); v1[j] = __builtin_amdgcn_exp2f(v1[j]); }
;                         v0 = v0 + 1.f; v1 = v1 + 1.f;
; #pragma unroll
;                         for (int j = 0; j < 4; ++j) { v0[j] = __builtin_amdgcn_rcpf(v0[j]); v1[j] = __builtin_amdgcn_rcpf(v1[j]); }
;                         v0 = v0 * 255.f + 0.5f; v1 = v1 * 255.f + 0.5f;
;                         unsigned q[8];
; #pragma unroll
;                         for (int j = 0; j < 4; ++j) { q[j] = max((unsigned)v0[j], 1u); q[4 + j] = max((unsigned)v1[j], 1u); }
;                         u32x2 w; w.x = q[0] | (q[1] << 8) | (q[2] << 16) | (q[3] << 24); w.y = q[4] | (q[5] << 8) | (q[6] << 16) | (q[7] << 24);
;                         *(u32x2*)(G8 + (size_t)row * INW + u.pn * 256 + bj * 128 + wc * 32 + 8 * fq) = w;
;                     }
	v_max_u32_e32 v43, 1, v43
	v_pk_mul_f32 v[32:33], v[32:33], s[6:7] op_sel_hi:[1,0]
	v_pk_mul_f32 v[28:29], v[28:29], s[6:7] op_sel_hi:[1,0]
	v_pk_add_f32 v[30:31], v[30:31], 1.0 op_sel_hi:[1,0]
	v_pk_add_f32 v[26:27], v[26:27], 1.0 op_sel_hi:[1,0]
	v_max_u32_sdwa v47, v47, v228 dst_sel:WORD_1 dst_unused:UNUSED_PAD src0_sel:DWORD src1_sel:DWORD
	v_max_u32_sdwa v44, v44, v228 dst_sel:WORD_1 dst_unused:UNUSED_PAD src0_sel:DWORD src1_sel:DWORD
	v_max_u32_sdwa v48, v48, v228 dst_sel:BYTE_3 dst_unused:UNUSED_PAD src0_sel:DWORD src1_sel:DWORD
	v_max_u32_sdwa v45, v45, v228 dst_sel:BYTE_3 dst_unused:UNUSED_PAD src0_sel:DWORD src1_sel:DWORD
	v_lshl_or_b32 v42, v42, 8, v46
	v_lshl_or_b32 v43, v43, 8, v50
	v_exp_f32_e32 v32, v32
	v_exp_f32_e32 v33, v33
	v_exp_f32_e32 v28, v28
	v_exp_f32_e32 v29, v29
	v_rcp_f32_e32 v26, v26
	v_rcp_f32_e32 v31, v31
	v_pk_add_f32 v[22:23], v[22:23], v[134:135]
	v_pk_add_f32 v[18:19], v[18:19], v[130:131]
	v_or3_b32 v42, v42, v47, v48
	v_or3_b32 v43, v43, v44, v45
	v_fma_f32 v38, v38, s33, 0.5
	v_fma_f32 v35, v35, s33, 0.5
	v_pk_mul_f32 v[22:23], v[22:23], s[6:7] op_sel_hi:[1,0]
	v_pk_mul_f32 v[18:19], v[18:19], s[6:7] op_sel_hi:[1,0]
	global_store_dwordx2 v[106:107], v[42:43], off offset:128 nt
	v_cvt_u32_f32_e32 v38, v38
	v_cvt_u32_f32_e32 v35, v35
	v_max_u32_e32 v42, 1, v34
	v_max_u32_e32 v34, 1, v39
	v_fma_f32 v39, v40, s33, 0.5
	v_fma_f32 v36, v36, s33, 0.5
	v_fma_f32 v40, v41, s33, 0.5
	v_fma_f32 v37, v37, s33, 0.5
	v_exp_f32_e32 v22, v22
	v_exp_f32_e32 v18, v18
	v_exp_f32_e32 v23, v23
	v_exp_f32_e32 v19, v19
	v_cvt_u32_f32_e32 v39, v39
	v_cvt_u32_f32_e32 v36, v36
	v_cvt_u32_f32_e32 v40, v40
	v_cvt_u32_f32_e32 v37, v37
	v_pk_add_f32 v[32:33], v[32:33], 1.0 op_sel_hi:[1,0]
	v_pk_add_f32 v[28:29], v[28:29], 1.0 op_sel_hi:[1,0]
	v_rcp_f32_e32 v30, v30
	v_rcp_f32_e32 v27, v27
	v_fma_f32 v26, v26, s33, 0.5
	v_fma_f32 v31, v31, s33, 0.5
	v_rcp_f32_e32 v32, v32
	v_rcp_f32_e32 v28, v28
	v_rcp_f32_e32 v33, v33
	v_rcp_f32_e32 v29, v29
	v_cvt_u32_f32_e32 v26, v26
	v_cvt_u32_f32_e32 v31, v31
	v_pk_add_f32 v[24:25], v[24:25], v[136:137]
	v_pk_add_f32 v[20:21], v[20:21], v[132:133]
	v_max_u32_e32 v38, 1, v38
	v_max_u32_e32 v35, 1, v35
	v_pk_mul_f32 v[24:25], v[24:25], s[6:7] op_sel_hi:[1,0]
	v_pk_mul_f32 v[20:21], v[20:21], s[6:7] op_sel_hi:[1,0]
	v_pk_add_f32 v[22:23], v[22:23], 1.0 op_sel_hi:[1,0]
	v_pk_add_f32 v[18:19], v[18:19], 1.0 op_sel_hi:[1,0]
	v_max_u32_sdwa v39, v39, v228 dst_sel:WORD_1 dst_unused:UNUSED_PAD src0_sel:DWORD src1_sel:DWORD
	v_max_u32_sdwa v36, v36, v228 dst_sel:WORD_1 dst_unused:UNUSED_PAD src0_sel:DWORD src1_sel:DWORD
	v_max_u32_sdwa v40, v40, v228 dst_sel:BYTE_3 dst_unused:UNUSED_PAD src0_sel:DWORD src1_sel:DWORD
	v_max_u32_sdwa v37, v37, v228 dst_sel:BYTE_3 dst_unused:UNUSED_PAD src0_sel:DWORD src1_sel:DWORD
	v_lshl_or_b32 v34, v34, 8, v38
	v_lshl_or_b32 v35, v35, 8, v42
	v_exp_f32_e32 v24, v24
	v_exp_f32_e32 v25, v25
	v_exp_f32_e32 v20, v20
	v_exp_f32_e32 v21, v21
	v_rcp_f32_e32 v18, v18
	v_rcp_f32_e32 v23, v23
	v_pk_add_f32 v[14:15], v[14:15], v[134:135]
	v_pk_add_f32 v[10:11], v[10:11], v[130:131]
	v_or3_b32 v34, v34, v39, v40
	v_or3_b32 v35, v35, v36, v37
	v_fma_f32 v30, v30, s33, 0.5
	v_fma_f32 v27, v27, s33, 0.5
	v_pk_mul_f32 v[14:15], v[14:15], s[6:7] op_sel_hi:[1,0]
	v_pk_mul_f32 v[10:11], v[10:11], s[6:7] op_sel_hi:[1,0]
	global_store_dwordx2 v[98:99], v[34:35], off offset:128 nt
	v_cvt_u32_f32_e32 v30, v30
	v_cvt_u32_f32_e32 v27, v27
	v_max_u32_e32 v34, 1, v26
	v_max_u32_e32 v26, 1, v31
	v_fma_f32 v31, v32, s33, 0.5
	v_fma_f32 v28, v28, s33, 0.5
	v_fma_f32 v32, v33, s33, 0.5
	v_fma_f32 v29, v29, s33, 0.5
	v_exp_f32_e32 v14, v14
	v_exp_f32_e32 v10, v10
	v_exp_f32_e32 v15, v15
	v_exp_f32_e32 v11, v11
	v_cvt_u32_f32_e32 v31, v31
	v_cvt_u32_f32_e32 v28, v28
	v_cvt_u32_f32_e32 v32, v32
	v_cvt_u32_f32_e32 v29, v29
	v_pk_add_f32 v[24:25], v[24:25], 1.0 op_sel_hi:[1,0]
	v_pk_add_f32 v[20:21], v[20:21], 1.0 op_sel_hi:[1,0]
	v_rcp_f32_e32 v22, v22
	v_rcp_f32_e32 v19, v19
	v_fma_f32 v18, v18, s33, 0.5
	v_fma_f32 v23, v23, s33, 0.5
	v_rcp_f32_e32 v24, v24
	v_rcp_f32_e32 v20, v20
	v_rcp_f32_e32 v25, v25
	v_rcp_f32_e32 v21, v21
	v_cvt_u32_f32_e32 v18, v18
	v_cvt_u32_f32_e32 v23, v23
	v_pk_add_f32 v[16:17], v[16:17], v[136:137]
	v_pk_add_f32 v[12:13], v[12:13], v[132:133]
	v_max_u32_e32 v30, 1, v30
	v_max_u32_e32 v27, 1, v27
	v_pk_mul_f32 v[16:17], v[16:17], s[6:7] op_sel_hi:[1,0]
	v_pk_mul_f32 v[12:13], v[12:13], s[6:7] op_sel_hi:[1,0]
	v_pk_add_f32 v[14:15], v[14:15], 1.0 op_sel_hi:[1,0]
	v_pk_add_f32 v[10:11], v[10:11], 1.0 op_sel_hi:[1,0]
	v_max_u32_sdwa v31, v31, v228 dst_sel:WORD_1 dst_unused:UNUSED_PAD src0_sel:DWORD src1_sel:DWORD
	v_max_u32_sdwa v28, v28, v228 dst_sel:WORD_1 dst_unused:UNUSED_PAD src0_sel:DWORD src1_sel:DWORD
	v_max_u32_sdwa v32, v32, v228 dst_sel:BYTE_3 dst_unused:UNUSED_PAD src0_sel:DWORD src1_sel:DWORD
;     __device__ __forceinline__ void operator()(const AccT& acc, const gm::GUnit& u, int wr, int wc, int fr, int fq) const {
;     ...
;                     for (int m = 0; m < 4; ++m) {
;                         const int row = u.pm * 256 + ai * 128 + wr * 64 + m * 16 + fr;
;                         f32x4 v0 = (acc[ai][bj][m][0] + b0) * -1.4426950408889634f, v1 = (acc[ai][bj][m][1] + b1) * -1.4426950408889634f;
; #pragma unroll
;                         for (int j = 0; j < 4; ++j) { v0[j] = __builtin_amdgcn_exp2f(v0[j]); v1[j] = __builtin_amdgcn_exp2f(v1[j]); }
;                         v0 = v0 + 1.f; v1 = v1 + 1.f;
; #pragma unroll
;                         for (int j = 0; j < 4; ++j) { v0[j] = __builtin_amdgcn_rcpf(v0[j]); v1[j] = __builtin_amdgcn_rcpf(v1[j]); }
;                         v0 = v0 * 255.f + 0.5f; v1 = v1 * 255.f + 0.5f;
;                         unsigned q[8];
; #pragma unroll
;                         for (int j = 0; j < 4; ++j) { q[j] = max((unsigned)v0[j], 1u); q[4 + j] = max((unsigned)v1[j], 1u); }
;                         u32x2 w; w.x = q[0] | (q[1] << 8) | (q[2] << 16) | (q[3] << 24); w.y = q[4] | (q[5] << 8) | (q[6] << 16) | (q[7] << 24);
;                         *(u32x2*)(G8 + (size_t)row * INW + u.pn * 256 + bj * 128 + wc * 32 + 8 * fq) = w;
;                     }
	v_max_u32_sdwa v29, v29, v228 dst_sel:BYTE_3 dst_unused:UNUSED_PAD src0_sel:DWORD src1_sel:DWORD
	v_lshl_or_b32 v26, v26, 8, v30
	v_lshl_or_b32 v27, v27, 8, v34
	v_exp_f32_e32 v16, v16
	v_exp_f32_e32 v17, v17
	v_exp_f32_e32 v12, v12
	v_exp_f32_e32 v13, v13
	v_rcp_f32_e32 v10, v10
	v_rcp_f32_e32 v15, v15
	v_pk_add_f32 v[6:7], v[6:7], v[134:135]
	v_pk_add_f32 v[2:3], v[2:3], v[130:131]
	v_or3_b32 v26, v26, v31, v32
	v_or3_b32 v27, v27, v28, v29
	v_fma_f32 v22, v22, s33, 0.5
	v_fma_f32 v19, v19, s33, 0.5
	v_pk_mul_f32 v[6:7], v[6:7], s[6:7] op_sel_hi:[1,0]
	v_pk_mul_f32 v[2:3], v[2:3], s[6:7] op_sel_hi:[1,0]
	global_store_dwordx2 v[90:91], v[26:27], off offset:128 nt
	v_cvt_u32_f32_e32 v22, v22
	v_cvt_u32_f32_e32 v19, v19
	v_max_u32_e32 v26, 1, v18
	v_max_u32_e32 v18, 1, v23
	v_fma_f32 v23, v24, s33, 0.5
	v_fma_f32 v20, v20, s33, 0.5
	v_fma_f32 v24, v25, s33, 0.5
	v_fma_f32 v21, v21, s33, 0.5
	v_exp_f32_e32 v6, v6
	v_exp_f32_e32 v2, v2
	v_exp_f32_e32 v7, v7
	v_exp_f32_e32 v3, v3
	v_cvt_u32_f32_e32 v23, v23
	v_cvt_u32_f32_e32 v20, v20
	v_cvt_u32_f32_e32 v24, v24
	v_cvt_u32_f32_e32 v21, v21
	v_pk_add_f32 v[16:17], v[16:17], 1.0 op_sel_hi:[1,0]
	v_pk_add_f32 v[12:13], v[12:13], 1.0 op_sel_hi:[1,0]
	v_rcp_f32_e32 v14, v14
	v_rcp_f32_e32 v11, v11
	v_fma_f32 v10, v10, s33, 0.5
	v_fma_f32 v15, v15, s33, 0.5
	v_rcp_f32_e32 v16, v16
	v_rcp_f32_e32 v12, v12
	v_rcp_f32_e32 v17, v17
	v_rcp_f32_e32 v13, v13
	v_cvt_u32_f32_e32 v10, v10
	v_cvt_u32_f32_e32 v15, v15
	v_pk_add_f32 v[8:9], v[8:9], v[136:137]
	v_pk_add_f32 v[4:5], v[4:5], v[132:133]
	v_max_u32_e32 v22, 1, v22
	v_max_u32_e32 v19, 1, v19
	v_pk_mul_f32 v[8:9], v[8:9], s[6:7] op_sel_hi:[1,0]
	v_pk_mul_f32 v[4:5], v[4:5], s[6:7] op_sel_hi:[1,0]
	v_pk_add_f32 v[6:7], v[6:7], 1.0 op_sel_hi:[1,0]
	v_pk_add_f32 v[2:3], v[2:3], 1.0 op_sel_hi:[1,0]
	v_max_u32_sdwa v23, v23, v228 dst_sel:WORD_1 dst_unused:UNUSED_PAD src0_sel:DWORD src1_sel:DWORD
	v_max_u32_sdwa v20, v20, v228 dst_sel:WORD_1 dst_unused:UNUSED_PAD src0_sel:DWORD src1_sel:DWORD
	v_max_u32_sdwa v24, v24, v228 dst_sel:BYTE_3 dst_unused:UNUSED_PAD src0_sel:DWORD src1_sel:DWORD
	v_max_u32_sdwa v21, v21, v228 dst_sel:BYTE_3 dst_unused:UNUSED_PAD src0_sel:DWORD src1_sel:DWORD
	v_lshl_or_b32 v18, v18, 8, v22
	v_lshl_or_b32 v19, v19, 8, v26
	v_exp_f32_e32 v8, v8
	v_exp_f32_e32 v9, v9
	v_exp_f32_e32 v4, v4
	v_exp_f32_e32 v5, v5
	v_rcp_f32_e32 v2, v2
	v_rcp_f32_e32 v7, v7
	v_or3_b32 v18, v18, v23, v24
	v_or3_b32 v19, v19, v20, v21
	v_fma_f32 v14, v14, s33, 0.5
	v_fma_f32 v11, v11, s33, 0.5
	global_store_dwordx2 v[82:83], v[18:19], off offset:128 nt
	v_cvt_u32_f32_e32 v14, v14
	v_cvt_u32_f32_e32 v11, v11
	v_max_u32_e32 v18, 1, v10
	v_max_u32_e32 v10, 1, v15
	v_fma_f32 v15, v16, s33, 0.5
	v_fma_f32 v12, v12, s33, 0.5
	v_fma_f32 v16, v17, s33, 0.5
	v_fma_f32 v13, v13, s33, 0.5
	v_cvt_u32_f32_e32 v15, v15
	v_cvt_u32_f32_e32 v12, v12
	v_cvt_u32_f32_e32 v16, v16
	v_cvt_u32_f32_e32 v13, v13
	v_pk_add_f32 v[8:9], v[8:9], 1.0 op_sel_hi:[1,0]
	v_pk_add_f32 v[4:5], v[4:5], 1.0 op_sel_hi:[1,0]
	v_rcp_f32_e32 v6, v6
	v_rcp_f32_e32 v3, v3
	v_fma_f32 v2, v2, s33, 0.5
	v_fma_f32 v7, v7, s33, 0.5
	v_rcp_f32_e32 v8, v8
	v_rcp_f32_e32 v4, v4
	v_rcp_f32_e32 v9, v9
	v_rcp_f32_e32 v5, v5
	v_cvt_u32_f32_e32 v2, v2
	v_cvt_u32_f32_e32 v7, v7
	v_max_u32_e32 v14, 1, v14
	v_max_u32_e32 v11, 1, v11
	v_max_u32_sdwa v15, v15, v228 dst_sel:WORD_1 dst_unused:UNUSED_PAD src0_sel:DWORD src1_sel:DWORD
	v_max_u32_sdwa v12, v12, v228 dst_sel:WORD_1 dst_unused:UNUSED_PAD src0_sel:DWORD src1_sel:DWORD
	v_max_u32_sdwa v16, v16, v228 dst_sel:BYTE_3 dst_unused:UNUSED_PAD src0_sel:DWORD src1_sel:DWORD
	v_max_u32_sdwa v13, v13, v228 dst_sel:BYTE_3 dst_unused:UNUSED_PAD src0_sel:DWORD src1_sel:DWORD
	v_lshl_or_b32 v10, v10, 8, v14
	v_lshl_or_b32 v11, v11, 8, v18
	v_or3_b32 v10, v10, v15, v16
	v_or3_b32 v11, v11, v12, v13
	v_fma_f32 v6, v6, s33, 0.5
	v_fma_f32 v3, v3, s33, 0.5
	global_store_dwordx2 v[74:75], v[10:11], off offset:128 nt
	v_cvt_u32_f32_e32 v6, v6
	v_cvt_u32_f32_e32 v3, v3
	v_max_u32_e32 v10, 1, v2
	v_max_u32_e32 v2, 1, v7
	v_fma_f32 v7, v8, s33, 0.5
	v_fma_f32 v4, v4, s33, 0.5
	v_fma_f32 v8, v9, s33, 0.5
	v_fma_f32 v5, v5, s33, 0.5
	v_cvt_u32_f32_e32 v7, v7
	v_cvt_u32_f32_e32 v4, v4
	v_cvt_u32_f32_e32 v8, v8
	v_cvt_u32_f32_e32 v5, v5
	v_max_u32_e32 v6, 1, v6
	v_max_u32_e32 v3, 1, v3
	v_max_u32_sdwa v7, v7, v228 dst_sel:WORD_1 dst_unused:UNUSED_PAD src0_sel:DWORD src1_sel:DWORD
	v_max_u32_sdwa v4, v4, v228 dst_sel:WORD_1 dst_unused:UNUSED_PAD src0_sel:DWORD src1_sel:DWORD
	v_max_u32_sdwa v8, v8, v228 dst_sel:BYTE_3 dst_unused:UNUSED_PAD src0_sel:DWORD src1_sel:DWORD
	v_max_u32_sdwa v5, v5, v228 dst_sel:BYTE_3 dst_unused:UNUSED_PAD src0_sel:DWORD src1_sel:DWORD
	v_lshl_or_b32 v2, v2, 8, v6
	v_lshl_or_b32 v3, v3, 8, v10
	v_or3_b32 v2, v2, v7, v8
	v_or3_b32 v3, v3, v4, v5
	global_store_dwordx2 v[66:67], v[2:3], off offset:128 nt
	s_branch .LBB0_237
